# speedup vs baseline: 1.0047x; 1.0028x over previous
_Z11attn_kernelPKfS0_S0_PKcS2_PKDv4_jS0_S0_S0_S0_Pf:
	s_load_dwordx8 s[4:11], s[0:1], 0x0
	s_load_dwordx8 s[12:19], s[0:1], 0x20
	v_readfirstlane_b32 s20, v0
	s_bfe_u32 s28, s2, 0x10002
	s_lshr_b32 s29, s20, 6
	s_lshr_b32 s3, s20, 8
	s_bfe_u32 s30, s20, 0x20006
	s_lshr_b32 s31, s2, 3
	s_lshl_b32 s24, s28, 18
	s_waitcnt lgkmcnt(0)
	s_add_u32 s20, s10, s24
	s_addc_u32 s10, s11, 0
	s_and_b32 s21, s10, 0xffff
	s_add_u32 s24, s12, s24
	s_addc_u32 s10, s13, 0
	v_and_b32_e32 v1, 63, v0
	s_and_b32 s25, s10, 0xffff
	s_lshl_b32 s10, s30, 10
	s_lshl_b32 s38, s3, 12
	v_lshlrev_b32_e32 v2, 4, v1
	s_or_b32 s35, s10, s38
	v_lshl_or_b32 v2, s3, 17, v2
	s_cmp_lg_u32 0, -1
	v_or_b32_e32 v174, s10, v2
	s_cselect_b32 s10, 0, 0
	s_mov_b32 s36, 0
	s_mov_b32 s23, 0x20000
	s_mov_b32 s22, 0x40000
	s_add_i32 s33, s35, s10
	s_mov_b32 m0, s33
	s_nop 0
	buffer_load_dwordx4 v174, s[20:23], s36 offen lds
	s_mov_b32 s26, s22
	s_mov_b32 s27, s23
	s_add_i32 s34, s33, 0xc000
	s_mov_b32 m0, s34
	s_nop 0
	buffer_load_dwordx4 v174, s[24:27], s36 offen lds
	s_add_i32 s10, s33, 0x4000
	s_movk_i32 s37, 0x1000
	s_mov_b32 m0, s10
	s_nop 0
	buffer_load_dwordx4 v174, s[20:23], s37 offen lds
	s_add_i32 s10, s33, 0x8000
	s_movk_i32 s11, 0x2000
	s_mov_b32 m0, s10
	s_nop 0
	buffer_load_dwordx4 v174, s[20:23], s11 offen lds
	s_lshl_b32 s10, s2, 7
	s_and_b32 s10, s10, 0x380
	s_lshl_b32 s11, s31, 2
	s_add_i32 s10, s10, s11
	s_or_b32 s10, s30, s10
	v_and_b32_e32 v172, 31, v0
	v_lshl_or_b32 v140, s10, 7, v1
	v_mov_b32_e32 v141, 0
	v_lshl_add_u64 v[6:7], v[140:141], 4, s[14:15]
	v_ashrrev_i32_e32 v9, 31, v140
	v_mov_b32_e32 v8, v140
	v_lshl_or_b32 v140, s10, 5, v172
	v_lshlrev_b64 v[4:5], 2, v[140:141]
	v_lshl_add_u64 v[2:3], s[16:17], 0, v[4:5]
	global_load_dword v2, v[2:3], off
	v_lshl_add_u64 v[8:9], v[8:9], 4, s[14:15]
	global_load_dwordx4 v[116:119], v[6:7], off
	global_load_dwordx4 v[120:123], v[8:9], off offset:1024
	s_load_dwordx4 s[12:15], s[0:1], 0x40
	s_load_dwordx2 s[10:11], s[0:1], 0x50
	v_lshlrev_b32_e32 v173, 2, v1
	v_lshl_or_b32 v3, s28, 11, v173
	s_waitcnt lgkmcnt(0)
	global_load_dword v44, v3, s[14:15] offset:256
	global_load_dword v45, v3, s[14:15]
	v_bfe_u32 v175, v0, 5, 1
	v_lshlrev_b32_e32 v0, 11, v175
	v_lshlrev_b32_e32 v3, 4, v172
	s_add_i32 s0, s38, 0
	v_lshl_add_u64 v[4:5], s[12:13], 0, v[4:5]
	v_add3_u32 v176, s0, v0, v3
	global_load_dword v0, v[4:5], off
	v_lshrrev_b32_e32 v124, 2, v1
	v_lshrrev_b32_e32 v125, 4, v1
	v_xor_b32_e32 v124, v124, v125
	v_and_b32_e32 v124, 1, v124
	v_add_u32_e32 v124, -1, v124
	v_and_b32_e32 v124, 0x38383838, v124
	v_mov_b32_e32 v200, 0
	v_mov_b32_e32 v201, 0
	v_mov_b32_e32 v202, 0
	v_mov_b32_e32 v203, 0
	v_mov_b32_e32 v204, 0
	v_mov_b32_e32 v125, v124
	v_mov_b32_e32 v126, v124
	v_mov_b32_e32 v127, v124
	v_mov_b32_e32 v128, v124
	v_mov_b32_e32 v129, v124
	v_mov_b32_e32 v130, v124
	v_mov_b32_e32 v131, v124
	v_mov_b32_e32 v140, 0x7f7f7f7f
	s_mov_b32 s0, 0xf800000
	s_movk_i32 s15, 0x3000
	s_mov_b32 s12, 1
	s_movk_i32 s14, 0x4000
	s_mov_b32 s13, 0x8000
	v_mov_b32_e32 v132, v141
	v_mov_b32_e32 v133, v141
	v_mov_b32_e32 v134, v141
	v_mov_b32_e32 v135, v141
	v_mov_b32_e32 v136, v141
	v_mov_b32_e32 v137, v141
	v_mov_b32_e32 v138, v141
	v_mov_b32_e32 v139, v141
	s_waitcnt vmcnt(5)
	v_mov_b32_e32 v4, v2
	v_mov_b32_e32 v5, v2
	v_mov_b32_e32 v6, v2
	v_mov_b32_e32 v7, v2
	v_mov_b32_e32 v8, v2
	v_mov_b32_e32 v9, v2
	v_mov_b32_e32 v10, v2
	v_mov_b32_e32 v11, v2
	v_mov_b32_e32 v12, v2
	v_mov_b32_e32 v13, v2
	v_mov_b32_e32 v14, v2
	v_mov_b32_e32 v15, v2
	v_mov_b32_e32 v16, v2
	v_mov_b32_e32 v17, v2
	v_mov_b32_e32 v3, v2
	v_mov_b64_e32 v[18:19], v[16:17]
	v_mov_b64_e32 v[16:17], v[14:15]
	v_mov_b64_e32 v[14:15], v[12:13]
	v_mov_b64_e32 v[12:13], v[10:11]
	v_mov_b64_e32 v[10:11], v[8:9]
	v_mov_b64_e32 v[8:9], v[6:7]
	v_mov_b64_e32 v[6:7], v[4:5]
	v_mov_b64_e32 v[4:5], v[2:3]
	s_waitcnt vmcnt(0) lgkmcnt(0)
	s_barrier
	ds_read_b128 v[24:27], v176 offset:1024
	ds_read_b128 v[20:23], v176
	ds_read_b128 v[36:39], v176 offset:512
	ds_read_b128 v[40:43], v176 offset:1536
	ds_read_b128 v[84:87], v176 offset:16384
	ds_read_b128 v[92:95], v176 offset:16896
	ds_read_b128 v[88:91], v176 offset:17408
	ds_read_b128 v[96:99], v176 offset:17920
	s_waitcnt vmcnt(3) lgkmcnt(6)
	v_mfma_f32_32x32x64_f8f6f4 v[20:35], v[20:27], v[116:123], v[4:19]
	s_waitcnt vmcnt(2)
	v_max_f32_e32 v3, v44, v44
	s_waitcnt vmcnt(1)
	v_max_f32_e32 v44, v45, v45
	v_max_f32_e32 v44, v44, v3
	s_nop 1
	v_max_f32_dpp v44, v44, v44 quad_perm:[1,0,3,2] row_mask:0xf bank_mask:0xf
	s_nop 1
	v_max_f32_dpp v44, v44, v44 quad_perm:[2,3,0,1] row_mask:0xf bank_mask:0xf
	s_nop 1
	v_max_f32_dpp v44, v44, v44 row_half_mirror row_mask:0xf bank_mask:0xf
	s_nop 1
	v_max_f32_dpp v44, v44, v44 row_mirror row_mask:0xf bank_mask:0xf
	s_nop 1
	v_max_f32_dpp v44, v44, v44 row_bcast:15 row_mask:0xa bank_mask:0xf
	s_nop 1
	v_max_f32_dpp v44, v44, v44 row_bcast:31 row_mask:0xc bank_mask:0xf
	s_nop 1
	v_readlane_b32 s47, v44, 63
	s_waitcnt vmcnt(0) lgkmcnt(0)
	s_barrier
	v_mfma_f32_32x32x64_f8f6f4 v[4:19], v[36:43], v[116:123], v[4:19]
	s_mov_b32 m0, s33
	s_nop 0
	buffer_load_dwordx4 v174, s[20:23], s15 offen lds
	s_add_i32 s15, s34, 0x4000
	s_mov_b32 m0, s15
	s_nop 0
	buffer_load_dwordx4 v174, s[24:27], s37 offen lds
	s_nop 1
	v_max_f32_e32 v3, v21, v21
	v_max_f32_e32 v36, v20, v20
	v_max_f32_e32 v3, v36, v3
	s_nop 7
	v_max3_f32 v37, v22, v23, v5
	v_max3_f32 v36, v37, v26, v27
	v_max3_f32 v3, v3, v4, v6
	v_max3_f32 v3, v3, v7, v24
	v_max3_f32 v36, v36, v10, v11
	v_max3_f32 v3, v3, v25, v8
	v_max3_f32 v36, v36, v30, v31
	v_max3_f32 v3, v3, v9, v28
	v_max3_f32 v36, v36, v14, v15
	v_max3_f32 v3, v3, v29, v12
	v_max3_f32 v36, v36, v34, v35
	v_max3_f32 v3, v3, v13, v32
	v_max3_f32 v36, v36, v18, v19
	v_max3_f32 v3, v3, v33, v16
	v_max3_f32 v3, v3, v17, v36
	v_mov_b32_e32 v36, v3
	s_nop 1
	v_permlane32_swap_b32_e32 v3, v36
	v_max_f32_e32 v36, v36, v36
	v_max_f32_e32 v3, v3, v3
	v_max_f32_e32 v3, v3, v36
	v_sub_f32_e32 v36, 0xc0400000, v3
	v_pk_add_f32 v[20:21], v[36:37], v[20:21] op_sel_hi:[0,1]
	v_pk_add_f32 v[22:23], v[36:37], v[22:23] op_sel_hi:[0,1]
	v_pk_add_f32 v[24:25], v[36:37], v[24:25] op_sel_hi:[0,1]
	v_pk_add_f32 v[26:27], v[36:37], v[26:27] op_sel_hi:[0,1]
	v_pk_add_f32 v[28:29], v[36:37], v[28:29] op_sel_hi:[0,1]
	v_mov_b32_e32 v37, s47
	v_mul_f32_e32 v38, 0x4f800000, v37
	v_cmp_gt_f32_e32 vcc, s0, v37
	v_pk_add_f32 v[30:31], v[36:37], v[30:31] op_sel_hi:[0,1]
	v_cndmask_b32_e32 v37, v37, v38, vcc
	v_sqrt_f32_e32 v38, v37
	v_pk_add_f32 v[32:33], v[36:37], v[32:33] op_sel_hi:[0,1]
	v_pk_add_f32 v[34:35], v[36:37], v[34:35] op_sel_hi:[0,1]
	v_pk_add_f32 v[4:5], v[36:37], v[4:5] op_sel_hi:[0,1]
	v_pk_add_f32 v[6:7], v[36:37], v[6:7] op_sel_hi:[0,1]
	v_pk_add_f32 v[8:9], v[36:37], v[8:9] op_sel_hi:[0,1]
	v_pk_add_f32 v[10:11], v[36:37], v[10:11] op_sel_hi:[0,1]
	v_pk_add_f32 v[12:13], v[36:37], v[12:13] op_sel_hi:[0,1]
	v_pk_add_f32 v[14:15], v[36:37], v[14:15] op_sel_hi:[0,1]
	v_pk_add_f32 v[16:17], v[36:37], v[16:17] op_sel_hi:[0,1]
	v_pk_add_f32 v[18:19], v[36:37], v[18:19] op_sel_hi:[0,1]
	v_add_u32_e32 v36, -1, v38
	v_fma_f32 v39, -v36, v38, v37
	v_cmp_ge_f32_e64 s[0:1], 0, v39
	v_add_u32_e32 v39, 1, v38
	v_exp_f32_e32 v161, v20
	v_cndmask_b32_e64 v36, v38, v36, s[0:1]
	v_fma_f32 v38, -v39, v38, v37
	v_cmp_lt_f32_e64 s[0:1], 0, v38
	v_exp_f32_e32 v100, v4
	v_exp_f32_e32 v163, v21
	v_cndmask_b32_e64 v36, v36, v39, s[0:1]
	v_mul_f32_e32 v38, 0x37800000, v36
	v_cndmask_b32_e32 v36, v36, v38, vcc
	v_mov_b32_e32 v38, 0x260
	v_cmp_class_f32_e32 vcc, v37, v38
	s_mov_b32 s0, 0x42700000
	v_exp_f32_e32 v148, v5
	v_cndmask_b32_e32 v36, v36, v37, vcc
	s_waitcnt vmcnt(0)
	v_mul_f32_e32 v0, v36, v0
	v_mul_f32_e32 v0, 0x3f91eb85, v0
	v_exp_f32_e32 v162, v22
	v_exp_f32_e32 v101, v6
	v_exp_f32_e32 v164, v23
	v_exp_f32_e32 v102, v7
	v_exp_f32_e32 v150, v24
	v_exp_f32_e32 v143, v8
	v_exp_f32_e32 v154, v25
	v_exp_f32_e32 v146, v9
	v_exp_f32_e32 v152, v26
	v_exp_f32_e32 v145, v10
	v_exp_f32_e32 v157, v27
	v_exp_f32_e32 v147, v11
	v_exp_f32_e32 v149, v28
	v_exp_f32_e32 v69, v12
	v_exp_f32_e32 v153, v29
	v_exp_f32_e32 v109, v13
	v_exp_f32_e32 v151, v30
	v_exp_f32_e32 v108, v14
	v_exp_f32_e32 v156, v31
	v_exp_f32_e32 v142, v15
	v_exp_f32_e32 v155, v32
	v_exp_f32_e32 v110, v16
	v_exp_f32_e32 v159, v33
	v_exp_f32_e32 v144, v17
	v_exp_f32_e32 v158, v34
	v_exp_f32_e32 v111, v18
	v_exp_f32_e32 v160, v35
	v_exp_f32_e32 v114, v19
	v_cmp_nge_f32_e64 s[0:1], s0, v0
	v_sub_f32_e32 v0, v2, v3
	v_add_f32_e32 v36, 0xc0400000, v0
	v_mov_b32_e32 v37, v36
	v_mov_b32_e32 v38, v36
	v_mov_b32_e32 v39, v36
	v_mov_b32_e32 v40, v36
	v_mov_b32_e32 v41, v36
	v_mov_b32_e32 v42, v36
	v_mov_b32_e32 v43, v36
	v_mov_b32_e32 v44, v36
	v_mov_b32_e32 v45, v36
	v_mov_b32_e32 v46, v36
	v_mov_b32_e32 v47, v36
	v_mov_b32_e32 v48, v36
	v_mov_b32_e32 v49, v36
	v_mov_b32_e32 v50, v36
	v_mov_b32_e32 v51, v36
	v_mov_b32_e32 v4, v141
	v_mov_b32_e32 v5, v141
	v_mov_b32_e32 v6, v141
	v_mov_b32_e32 v7, v141
	v_mov_b32_e32 v8, v141
	v_mov_b32_e32 v9, v141
	v_mov_b32_e32 v10, v141
	v_mov_b32_e32 v11, v141
	v_mov_b32_e32 v12, v141
	v_mov_b32_e32 v13, v141
	v_mov_b32_e32 v14, v141
	v_mov_b32_e32 v15, v141
	v_mov_b32_e32 v16, v141
	v_mov_b32_e32 v17, v141
	v_mov_b32_e32 v18, v141
	v_mov_b32_e32 v19, v141
	v_mov_b32_e32 v20, v141
	v_mov_b32_e32 v21, v141
	v_mov_b32_e32 v22, v141
	v_mov_b32_e32 v23, v141
	v_mov_b32_e32 v24, v141
	v_mov_b32_e32 v25, v141
	v_mov_b32_e32 v26, v141
	v_mov_b32_e32 v27, v141
	v_mov_b32_e32 v28, v141
	v_mov_b32_e32 v29, v141
	v_mov_b32_e32 v30, v141
	v_mov_b32_e32 v31, v141
	v_mov_b32_e32 v32, v141
	v_mov_b32_e32 v33, v141
	v_mov_b32_e32 v34, v141
	v_mov_b32_e32 v35, v141
	v_mov_b32_e32 v0, v141
